# v49 + near-tie blocks moved out of line (common path of phase 3 is straight-line, branches inverted)
# speedup vs baseline: 1.0065x; 1.0065x over previous
.LBB0_118:
	s_waitcnt vmcnt(0)
	v_lshrrev_b32_e32 v67, 4, v0
	v_mov_b32_e32 v66, 0x11100
	v_lshl_or_b32 v66, v67, 2, v66
	s_waitcnt lgkmcnt(0)
	s_barrier
	ds_read_b32 v66, v66
	v_mul_u32_u24_e32 v68, 0x102, v67
	v_lshlrev_b32_e32 v72, 3, v68
	s_waitcnt lgkmcnt(0)
	v_max_i32_e32 v66, 1, v66
	v_cvt_f32_u32_e32 v66, v66
	v_div_scale_f32 v69, s[0:1], v66, v66, 1.0
	v_rcp_f32_e32 v70, v69
	v_div_scale_f32 v68, vcc, 1.0, v66, 1.0
	v_fma_f32 v71, -v69, v70, 1.0
	v_fmac_f32_e32 v70, v71, v70
	v_mul_f32_e32 v71, v68, v70
	v_fma_f32 v73, -v69, v71, v68
	v_fmac_f32_e32 v71, v73, v70
	v_fma_f32 v68, -v69, v71, v68
	v_div_fmas_f32 v73, v68, v70, v71
	v_lshl_add_u32 v68, v138, 3, v72
	v_add_u32_e32 v76, 0x8000, v68
	ds_read2_b64 v[68:71], v76 offset1:16
	v_div_fixup_f32 v77, v73, v66, 1.0
	v_mul_i32_i24_e32 v73, 0xfffffbf8, v67
	v_lshlrev_b32_e32 v66, 2, v138
	v_add3_u32 v78, v72, v73, v66
	ds_read2_b64 v[72:75], v76 offset0:32 offset1:48
	s_waitcnt lgkmcnt(1)
	v_cvt_f32_f64_e32 v68, v[68:69]
	v_cvt_f32_f64_e32 v69, v[70:71]
	v_mul_f32_e32 v68, v77, v68
	v_mul_f32_e32 v69, v77, v69
	v_fma_f32 v79, v68, v68, 0
	ds_write2_b32 v78, v68, v69 offset1:16
	s_waitcnt lgkmcnt(1)
	v_cvt_f32_f64_e32 v68, v[72:73]
	v_fmac_f32_e32 v79, v69, v69
	v_mul_f32_e32 v72, v77, v68
	ds_read2_b64 v[68:71], v76 offset0:64 offset1:80
	v_cvt_f32_f64_e32 v73, v[74:75]
	v_fmac_f32_e32 v79, v72, v72
	v_mul_f32_e32 v73, v77, v73
	v_fmac_f32_e32 v79, v73, v73
	ds_write2_b32 v78, v72, v73 offset0:32 offset1:48
	ds_read2_b64 v[72:75], v76 offset0:96 offset1:112
	s_waitcnt lgkmcnt(2)
	v_cvt_f32_f64_e32 v68, v[68:69]
	v_cvt_f32_f64_e32 v69, v[70:71]
	v_mul_f32_e32 v68, v77, v68
	v_mul_f32_e32 v69, v77, v69
	v_fmac_f32_e32 v79, v68, v68
	ds_write2_b32 v78, v68, v69 offset0:64 offset1:80
	s_waitcnt lgkmcnt(1)
	v_cvt_f32_f64_e32 v68, v[72:73]
	v_fmac_f32_e32 v79, v69, v69
	v_mul_f32_e32 v72, v77, v68
	ds_read2_b64 v[68:71], v76 offset0:128 offset1:144
	v_cvt_f32_f64_e32 v73, v[74:75]
	v_fmac_f32_e32 v79, v72, v72
	v_mul_f32_e32 v73, v77, v73
	v_fmac_f32_e32 v79, v73, v73
	ds_write2_b32 v78, v72, v73 offset0:96 offset1:112
	ds_read2_b64 v[72:75], v76 offset0:160 offset1:176
	s_waitcnt lgkmcnt(2)
	v_cvt_f32_f64_e32 v68, v[68:69]
	v_cvt_f32_f64_e32 v69, v[70:71]
	v_mul_f32_e32 v68, v77, v68
	v_mul_f32_e32 v69, v77, v69
	v_fmac_f32_e32 v79, v68, v68
	ds_write2_b32 v78, v68, v69 offset0:128 offset1:144
	s_waitcnt lgkmcnt(1)
	v_cvt_f32_f64_e32 v68, v[72:73]
	v_fmac_f32_e32 v79, v69, v69
	v_mul_f32_e32 v72, v77, v68
	ds_read2_b64 v[68:71], v76 offset0:192 offset1:208
	v_cvt_f32_f64_e32 v73, v[74:75]
	v_fmac_f32_e32 v79, v72, v72
	v_mul_f32_e32 v73, v77, v73
	v_fmac_f32_e32 v79, v73, v73
	ds_write2_b32 v78, v72, v73 offset0:160 offset1:176
	ds_read2_b64 v[72:75], v76 offset0:224 offset1:240
	s_waitcnt lgkmcnt(2)
	v_cvt_f32_f64_e32 v68, v[68:69]
	v_cvt_f32_f64_e32 v69, v[70:71]
	v_mul_f32_e32 v68, v77, v68
	v_mul_f32_e32 v69, v77, v69
	v_fmac_f32_e32 v79, v68, v68
	ds_write2_b32 v78, v68, v69 offset0:192 offset1:208
	s_waitcnt lgkmcnt(1)
	v_cvt_f32_f64_e32 v68, v[72:73]
	v_fmac_f32_e32 v79, v69, v69
	v_mul_f32_e32 v68, v77, v68
	v_cvt_f32_f64_e32 v69, v[74:75]
	v_fmac_f32_e32 v79, v68, v68
	v_mul_f32_e32 v69, v77, v69
	v_fmac_f32_e32 v79, v69, v69
	ds_write2_b32 v78, v68, v69 offset0:224 offset1:240
	v_cmp_eq_u32_e32 vcc, 0, v138
	v_add_f32_dpp v68, v79, v79 quad_perm:[1,0,3,2] row_mask:0xf bank_mask:0xf bound_ctrl:1
	s_nop 1
	v_add_f32_dpp v68, v68, v68 quad_perm:[2,3,0,1] row_mask:0xf bank_mask:0xf bound_ctrl:1
	s_nop 1
	v_add_f32_dpp v68, v68, v68 row_half_mirror row_mask:0xf bank_mask:0xf bound_ctrl:1
	s_nop 1
	v_mov_b32_dpp v69, v68 row_mirror row_mask:0xf bank_mask:0xf bound_ctrl:1
	s_and_saveexec_b64 s[0:1], vcc
	v_mov_b32_e32 v70, 0x11200
	v_lshl_or_b32 v67, v67, 2, v70
	v_add_f32_e32 v68, v68, v69
	ds_write_b32 v67, v68
	s_or_b64 exec, exec, s[0:1]
	v_lshlrev_b32_e32 v67, 2, v140
	s_movk_i32 s0, 0x408
	v_mad_u32_u24 v67, v138, s0, v67
	s_waitcnt lgkmcnt(0)
	s_barrier
	ds_read2_b32 v[68:69], v67 offset1:4
	ds_read2_b32 v[70:71], v67 offset0:64 offset1:68
	ds_read2_b32 v[72:73], v67 offset0:192 offset1:196
	s_lshl_b32 s29, s17, 2
	s_lshl_b32 s0, s24, 2
	s_waitcnt lgkmcnt(2)
	v_mfma_f32_16x16x4_f32 a[0:3], v68, v62, 0
	s_add_i32 s0, s0, 0x10100
	s_waitcnt lgkmcnt(1)
	v_mfma_f32_16x16x4_f32 a[4:7], v70, v63, 0
	ds_read2_b32 v[62:63], v67 offset0:128 offset1:132
	s_waitcnt lgkmcnt(0)
	v_mfma_f32_16x16x4_f32 a[0:3], v62, v64, a[0:3]
	v_mfma_f32_16x16x4_f32 a[4:7], v72, v65, a[4:7]
	v_mfma_f32_16x16x4_f32 a[0:3], v69, v58, a[0:3]
	v_mfma_f32_16x16x4_f32 a[4:7], v71, v59, a[4:7]
	ds_read2_b32 v[58:59], v67 offset0:8 offset1:12
	v_mfma_f32_16x16x4_f32 a[0:3], v63, v60, a[0:3]
	ds_read2_b32 v[62:63], v67 offset0:200 offset1:204
	v_mfma_f32_16x16x4_f32 a[4:7], v73, v61, a[4:7]
	ds_read2_b32 v[60:61], v67 offset0:72 offset1:76
	s_waitcnt lgkmcnt(2)
	v_mfma_f32_16x16x4_f32 a[0:3], v58, v54, a[0:3]
	s_waitcnt lgkmcnt(0)
	v_mfma_f32_16x16x4_f32 a[4:7], v60, v55, a[4:7]
	ds_read2_b32 v[54:55], v67 offset0:136 offset1:140
	s_waitcnt lgkmcnt(0)
	v_mfma_f32_16x16x4_f32 a[0:3], v54, v56, a[0:3]
	v_mfma_f32_16x16x4_f32 a[4:7], v62, v57, a[4:7]
	v_mfma_f32_16x16x4_f32 a[0:3], v59, v50, a[0:3]
	v_mfma_f32_16x16x4_f32 a[4:7], v61, v51, a[4:7]
	ds_read2_b32 v[50:51], v67 offset0:16 offset1:20
	v_mfma_f32_16x16x4_f32 a[0:3], v55, v52, a[0:3]
	ds_read2_b32 v[54:55], v67 offset0:208 offset1:212
	v_mfma_f32_16x16x4_f32 a[4:7], v63, v53, a[4:7]
	ds_read2_b32 v[52:53], v67 offset0:80 offset1:84
	s_waitcnt lgkmcnt(2)
	v_mfma_f32_16x16x4_f32 a[0:3], v50, v46, a[0:3]
	s_waitcnt lgkmcnt(0)
	v_mfma_f32_16x16x4_f32 a[4:7], v52, v47, a[4:7]
	ds_read2_b32 v[46:47], v67 offset0:144 offset1:148
	s_waitcnt lgkmcnt(0)
	v_mfma_f32_16x16x4_f32 a[0:3], v46, v48, a[0:3]
	v_mfma_f32_16x16x4_f32 a[4:7], v54, v49, a[4:7]
	v_mfma_f32_16x16x4_f32 a[0:3], v51, v42, a[0:3]
	v_mfma_f32_16x16x4_f32 a[4:7], v53, v43, a[4:7]
	ds_read2_b32 v[42:43], v67 offset0:24 offset1:28
	v_mfma_f32_16x16x4_f32 a[0:3], v47, v44, a[0:3]
	ds_read2_b32 v[46:47], v67 offset0:216 offset1:220
	v_mfma_f32_16x16x4_f32 a[4:7], v55, v45, a[4:7]
	ds_read2_b32 v[44:45], v67 offset0:88 offset1:92
	s_waitcnt lgkmcnt(2)
	v_mfma_f32_16x16x4_f32 a[0:3], v42, v38, a[0:3]
	s_waitcnt lgkmcnt(0)
	v_mfma_f32_16x16x4_f32 a[4:7], v44, v39, a[4:7]
	ds_read2_b32 v[38:39], v67 offset0:152 offset1:156
	s_waitcnt lgkmcnt(0)
	v_mfma_f32_16x16x4_f32 a[0:3], v38, v40, a[0:3]
	v_mfma_f32_16x16x4_f32 a[4:7], v46, v41, a[4:7]
	v_mfma_f32_16x16x4_f32 a[0:3], v43, v34, a[0:3]
	v_mfma_f32_16x16x4_f32 a[4:7], v45, v35, a[4:7]
	ds_read2_b32 v[34:35], v67 offset0:32 offset1:36
	v_mfma_f32_16x16x4_f32 a[0:3], v39, v36, a[0:3]
	ds_read2_b32 v[38:39], v67 offset0:224 offset1:228
	v_mfma_f32_16x16x4_f32 a[4:7], v47, v37, a[4:7]
	ds_read2_b32 v[36:37], v67 offset0:96 offset1:100
	s_waitcnt lgkmcnt(2)
	v_mfma_f32_16x16x4_f32 a[0:3], v34, v30, a[0:3]
	s_waitcnt lgkmcnt(0)
	v_mfma_f32_16x16x4_f32 a[4:7], v36, v31, a[4:7]
	ds_read2_b32 v[30:31], v67 offset0:160 offset1:164
	s_waitcnt lgkmcnt(0)
	v_mfma_f32_16x16x4_f32 a[0:3], v30, v32, a[0:3]
	v_mfma_f32_16x16x4_f32 a[4:7], v38, v33, a[4:7]
	v_mfma_f32_16x16x4_f32 a[0:3], v35, v26, a[0:3]
	v_mfma_f32_16x16x4_f32 a[4:7], v37, v27, a[4:7]
	ds_read2_b32 v[26:27], v67 offset0:40 offset1:44
	v_mfma_f32_16x16x4_f32 a[0:3], v31, v28, a[0:3]
	ds_read2_b32 v[30:31], v67 offset0:232 offset1:236
	v_mfma_f32_16x16x4_f32 a[4:7], v39, v29, a[4:7]
	ds_read2_b32 v[28:29], v67 offset0:104 offset1:108
	s_waitcnt lgkmcnt(2)
	v_mfma_f32_16x16x4_f32 a[0:3], v26, v22, a[0:3]
	s_waitcnt lgkmcnt(0)
	v_mfma_f32_16x16x4_f32 a[4:7], v28, v23, a[4:7]
	ds_read2_b32 v[22:23], v67 offset0:168 offset1:172
	s_waitcnt lgkmcnt(0)
	v_mfma_f32_16x16x4_f32 a[0:3], v22, v24, a[0:3]
	v_mfma_f32_16x16x4_f32 a[4:7], v30, v25, a[4:7]
	v_mfma_f32_16x16x4_f32 a[0:3], v27, v18, a[0:3]
	v_mfma_f32_16x16x4_f32 a[4:7], v29, v19, a[4:7]
	ds_read2_b32 v[18:19], v67 offset0:48 offset1:52
	v_mfma_f32_16x16x4_f32 a[0:3], v23, v20, a[0:3]
	ds_read2_b32 v[22:23], v67 offset0:240 offset1:244
	v_mfma_f32_16x16x4_f32 a[4:7], v31, v21, a[4:7]
	ds_read2_b32 v[20:21], v67 offset0:112 offset1:116
	s_waitcnt lgkmcnt(2)
	v_mfma_f32_16x16x4_f32 a[0:3], v18, v14, a[0:3]
	s_waitcnt lgkmcnt(0)
	v_mfma_f32_16x16x4_f32 a[4:7], v20, v15, a[4:7]
	ds_read2_b32 v[14:15], v67 offset0:176 offset1:180
	s_waitcnt lgkmcnt(0)
	v_mfma_f32_16x16x4_f32 a[0:3], v14, v16, a[0:3]
	v_mfma_f32_16x16x4_f32 a[4:7], v22, v17, a[4:7]
	v_mfma_f32_16x16x4_f32 a[0:3], v19, v10, a[0:3]
	v_mfma_f32_16x16x4_f32 a[4:7], v21, v11, a[4:7]
	ds_read2_b32 v[10:11], v67 offset0:56 offset1:60
	v_mfma_f32_16x16x4_f32 a[0:3], v15, v12, a[0:3]
	ds_read2_b32 v[14:15], v67 offset0:248 offset1:252
	v_mfma_f32_16x16x4_f32 a[4:7], v23, v13, a[4:7]
	ds_read2_b32 v[12:13], v67 offset0:120 offset1:124
	s_waitcnt lgkmcnt(2)
	v_mfma_f32_16x16x4_f32 a[0:3], v10, v6, a[0:3]
	s_waitcnt lgkmcnt(0)
	v_mfma_f32_16x16x4_f32 a[4:7], v12, v7, a[4:7]
	ds_read2_b32 v[6:7], v67 offset0:184 offset1:188
	s_waitcnt lgkmcnt(0)
	v_mfma_f32_16x16x4_f32 a[0:3], v6, v8, a[0:3]
	v_mfma_f32_16x16x4_f32 a[4:7], v14, v9, a[4:7]
	v_mfma_f32_16x16x4_f32 a[0:3], v11, v2, a[0:3]
	v_mov_b32_e32 v2, 0x11300
	v_lshl_add_u32 v2, v134, 2, v2
	ds_read_b32 v2, v2
	v_mfma_f32_16x16x4_f32 a[4:7], v13, v3, a[4:7]
	v_lshlrev_b32_e32 v3, 10, v140
	v_add3_u32 v3, s0, v66, v3
	v_mfma_f32_16x16x4_f32 a[0:3], v7, v4, a[0:3]
	v_or_b32_e32 v7, s29, v140
	v_lshl_or_b32 v4, v7, 8, v66
	v_add_u32_e32 v4, 0x10100, v4
	v_mfma_f32_16x16x4_f32 a[4:7], v15, v5, a[4:7]
	s_nop 9
	v_accvgpr_read_b32 v5, a0
	v_accvgpr_read_b32 v6, a1
	v_accvgpr_read_b32 v8, a2
	v_accvgpr_read_b32 v9, a3
	v_accvgpr_read_b32 v70, a4
	v_accvgpr_read_b32 v71, a5
	v_accvgpr_read_b32 v72, a6
	v_accvgpr_read_b32 v73, a7
	v_add_f32_e32 v5, v5, v70
	v_add_f32_e32 v6, v6, v71
	v_add_f32_e32 v8, v8, v72
	v_add_f32_e32 v9, v9, v73
	s_waitcnt lgkmcnt(0)
	v_fma_f32 v5, -2.0, v5, v2
	v_fma_f32 v6, -2.0, v6, v2
	v_fma_f32 v8, -2.0, v8, v2
	v_fmac_f32_e32 v2, -2.0, v9
	ds_write2st64_b32 v3, v5, v6 offset1:1
	ds_write2st64_b32 v3, v8, v2 offset0:2 offset1:3
	s_waitcnt lgkmcnt(0)
	s_barrier
	ds_read2_b32 v[2:3], v4 offset1:16
	ds_read2_b32 v[4:5], v4 offset0:32 offset1:48
	v_or_b32_e32 v6, 16, v138
	v_or_b32_e32 v8, 32, v138
	v_or_b32_e32 v9, 48, v138
	s_waitcnt lgkmcnt(1)
	v_cmp_lt_f32_e32 vcc, v3, v2
	s_nop 1
	v_cndmask_b32_e32 v10, v2, v3, vcc
	v_cndmask_b32_e32 v6, v138, v6, vcc
	s_waitcnt lgkmcnt(0)
	v_cmp_lt_f32_e32 vcc, v4, v10
	s_nop 1
	v_cndmask_b32_e32 v10, v10, v4, vcc
	v_cndmask_b32_e32 v8, v6, v8, vcc
	v_cmp_lt_f32_e32 vcc, v5, v10
	s_nop 1
	v_cndmask_b32_e32 v6, v10, v5, vcc
	v_cndmask_b32_e32 v14, v8, v9, vcc
	s_nop 0
	v_mov_b32_dpp v9, v6 quad_perm:[1,0,3,2] row_mask:0xf bank_mask:0xf bound_ctrl:1
	v_mov_b32_dpp v8, v14 quad_perm:[1,0,3,2] row_mask:0xf bank_mask:0xf bound_ctrl:1
	v_cmp_gt_f32_e64 s[4:5], v6, v9
	v_cmp_ngt_f32_e32 vcc, v6, v9
	s_and_saveexec_b64 s[6:7], vcc
	v_cmp_eq_f32_e32 vcc, v6, v9
	v_cmp_lt_i32_e64 s[0:1], v8, v14
	s_and_b64 s[0:1], vcc, s[0:1]
	s_andn2_b64 s[4:5], s[4:5], exec
	s_and_b64 s[0:1], s[0:1], exec
	s_or_b64 s[4:5], s[4:5], s[0:1]
	s_or_b64 exec, exec, s[6:7]
	s_and_saveexec_b64 s[0:1], s[4:5]
	v_mov_b32_e32 v6, v9
	v_mov_b32_e32 v14, v8
	s_or_b64 exec, exec, s[0:1]
	v_mov_b32_dpp v9, v6 quad_perm:[2,3,0,1] row_mask:0xf bank_mask:0xf bound_ctrl:1
	v_mov_b32_dpp v8, v14 quad_perm:[2,3,0,1] row_mask:0xf bank_mask:0xf bound_ctrl:1
	v_cmp_gt_f32_e64 s[4:5], v6, v9
	v_cmp_ngt_f32_e32 vcc, v6, v9
	s_and_saveexec_b64 s[6:7], vcc
	v_cmp_eq_f32_e32 vcc, v6, v9
	v_cmp_lt_i32_e64 s[0:1], v8, v14
	s_and_b64 s[0:1], vcc, s[0:1]
	s_andn2_b64 s[4:5], s[4:5], exec
	s_and_b64 s[0:1], s[0:1], exec
	s_or_b64 s[4:5], s[4:5], s[0:1]
	s_or_b64 exec, exec, s[6:7]
	s_and_saveexec_b64 s[0:1], s[4:5]
	v_mov_b32_e32 v6, v9
	v_mov_b32_e32 v14, v8
	s_or_b64 exec, exec, s[0:1]
	v_mov_b32_dpp v9, v6 row_half_mirror row_mask:0xf bank_mask:0xf bound_ctrl:1
	v_mov_b32_dpp v8, v14 row_half_mirror row_mask:0xf bank_mask:0xf bound_ctrl:1
	v_cmp_gt_f32_e64 s[4:5], v6, v9
	v_cmp_ngt_f32_e32 vcc, v6, v9
	s_and_saveexec_b64 s[6:7], vcc
	v_cmp_eq_f32_e32 vcc, v6, v9
	v_cmp_lt_i32_e64 s[0:1], v8, v14
	s_and_b64 s[0:1], vcc, s[0:1]
	s_andn2_b64 s[4:5], s[4:5], exec
	s_and_b64 s[0:1], s[0:1], exec
	s_or_b64 s[4:5], s[4:5], s[0:1]
	s_or_b64 exec, exec, s[6:7]
	s_and_saveexec_b64 s[0:1], s[4:5]
	v_mov_b32_e32 v6, v9
	v_mov_b32_e32 v14, v8
	s_or_b64 exec, exec, s[0:1]
	v_mov_b32_dpp v8, v6 row_mirror row_mask:0xf bank_mask:0xf bound_ctrl:1
	v_mov_b32_dpp v9, v14 row_mirror row_mask:0xf bank_mask:0xf bound_ctrl:1
	v_cmp_gt_f32_e64 s[4:5], v6, v8
	v_cmp_ngt_f32_e32 vcc, v6, v8
	s_and_saveexec_b64 s[6:7], vcc
	v_cmp_eq_f32_e32 vcc, v6, v8
	v_cmp_lt_i32_e64 s[0:1], v9, v14
	s_and_b64 s[0:1], vcc, s[0:1]
	s_andn2_b64 s[4:5], s[4:5], exec
	s_and_b64 s[0:1], s[0:1], exec
	s_or_b64 s[4:5], s[4:5], s[0:1]
	s_or_b64 exec, exec, s[6:7]
	s_and_saveexec_b64 s[0:1], s[4:5]
	v_mov_b32_e32 v6, v8
	v_mov_b32_e32 v14, v9
	s_or_b64 exec, exec, s[0:1]
	v_mov_b32_e32 v8, 0x11300
	v_lshl_or_b32 v8, v1, 2, v8
	ds_read_b32 v8, v8
	v_mov_b32_e32 v9, 0x11200
	v_lshl_add_u32 v7, v7, 2, v9
	ds_read_b32 v9, v7
	v_mov_b32_e32 v13, 0x260
	s_waitcnt lgkmcnt(1)
	v_mov_b32_dpp v7, v8 quad_perm:[1,0,3,2] row_mask:0xf bank_mask:0xf bound_ctrl:1
	v_max_f32_e32 v8, v8, v8
	v_max_f32_e32 v7, v7, v7
	v_max_f32_e32 v7, v8, v7
	v_lshlrev_b32_e32 v18, 2, v139
	v_mov_b32_e32 v19, 0
	v_mov_b32_dpp v8, v7 quad_perm:[2,3,0,1] row_mask:0xf bank_mask:0xf bound_ctrl:1
	v_max_f32_e32 v8, v8, v8
	v_max_f32_e32 v7, v7, v8
	s_mov_b32 s25, 0
	s_mov_b32 s26, s25
	v_mov_b32_dpp v8, v7 row_half_mirror row_mask:0xf bank_mask:0xf bound_ctrl:1
	v_max_f32_e32 v8, v8, v8
	v_max_f32_e32 v7, v7, v8
	s_nop 1
	v_mov_b32_dpp v8, v7 row_mirror row_mask:0xf bank_mask:0xf bound_ctrl:1
	v_max_f32_e32 v8, v8, v8
	v_max_f32_e32 v7, v7, v8
	s_nop 0
	v_readlane_b32 s4, v7, 32
	v_readlane_b32 s5, v7, 48
	v_readlane_b32 s0, v7, 0
	v_readlane_b32 s1, v7, 16
	v_max_f32_e64 v7, s5, s5
	v_max_f32_e64 v8, s4, s4
	v_max_f32_e32 v7, v8, v7
	v_mov_b32_e32 v8, s1
	v_max3_f32 v8, s0, v8, v7
	s_mov_b32 s0, 0x3f800347
	s_mov_b32 s1, 0x3f8020c5
	s_waitcnt lgkmcnt(0)
	v_pk_mul_f32 v[8:9], v[8:9], s[0:1]
	s_mov_b32 s4, 0xf800000
	v_mul_f32_e32 v7, 0x4f800000, v9
	v_cmp_gt_f32_e32 vcc, s4, v9
	s_nop 1
	v_cndmask_b32_e32 v7, v9, v7, vcc
	v_sqrt_f32_e32 v10, v7
	s_nop 0
	v_add_u32_e32 v11, -1, v10
	v_fma_f32 v12, -v11, v10, v7
	v_cmp_ge_f32_e64 s[0:1], 0, v12
	v_add_u32_e32 v12, 1, v10
	s_nop 0
	v_cndmask_b32_e64 v11, v10, v11, s[0:1]
	v_fma_f32 v10, -v12, v10, v7
	v_cmp_lt_f32_e64 s[0:1], 0, v10
	s_nop 1
	v_cndmask_b32_e64 v10, v11, v12, s[0:1]
	v_mul_f32_e32 v11, 0x37800000, v10
	v_cndmask_b32_e32 v10, v10, v11, vcc
	v_mul_f32_e32 v11, 0x4f800000, v8
	v_cmp_gt_f32_e32 vcc, s4, v8
	v_cmp_class_f32_e64 s[0:1], v7, v13
	s_nop 0
	v_cndmask_b32_e32 v11, v8, v11, vcc
	v_sqrt_f32_e32 v12, v11
	v_cndmask_b32_e64 v7, v10, v7, s[0:1]
	v_add_u32_e32 v10, -1, v12
	v_fma_f32 v15, -v10, v12, v11
	v_cmp_ge_f32_e64 s[0:1], 0, v15
	v_add_u32_e32 v15, 1, v12
	s_nop 0
	v_cndmask_b32_e64 v10, v12, v10, s[0:1]
	v_fma_f32 v12, -v15, v12, v11
	v_cmp_lt_f32_e64 s[0:1], 0, v12
	s_nop 1
	v_cndmask_b32_e64 v10, v10, v15, s[0:1]
	v_mul_f32_e32 v12, 0x37800000, v10
	v_cndmask_b32_e32 v10, v10, v12, vcc
	v_cmp_class_f32_e32 vcc, v11, v13
	s_mov_b32 s0, 0x380637bd
	s_mov_b32 s1, 0x350637bd
	v_cndmask_b32_e32 v10, v10, v11, vcc
	v_mul_f32_e32 v7, v7, v10
	v_mul_f32_e32 v7, 0x3f800347, v7
	v_pk_mul_f32 v[8:9], v[8:9], s[0:1]
	s_nop 0
	v_fmamk_f32 v7, v7, 0x3888509c, v9
	v_add_f32_e32 v7, v8, v7
	v_add_f32_e32 v7, 0xda24260, v7
	v_add_f32_e32 v6, v6, v7
	v_cmp_le_f32_e64 s[8:9], v2, v6
	v_cmp_le_f32_e64 s[6:7], v3, v6
	v_cmp_le_f32_e64 s[4:5], v4, v6
	v_lshl_add_u64 v[2:3], s[22:23], 0, v[18:19]
	s_and_b32 s19, s8, 0xffff
	s_lshl_b32 s22, s6, 16
	v_cmp_le_f32_e64 s[0:1], v5, v6
	s_or_b32 s24, s19, s22
	s_and_b32 s23, s4, 0xffff
	s_mov_b32 s22, s25
	s_or_b64 s[22:23], s[24:25], s[22:23]
	s_lshl_b32 s27, s0, 16
	s_or_b64 s[26:27], s[22:23], s[26:27]
	s_add_u32 s22, s26, -1
	s_addc_u32 s23, s27, -1
	s_and_b64 s[22:23], s[26:27], s[22:23]
	s_cmp_eq_u64 s[22:23], 0
	v_readlane_b32 s22, v14, 0
	s_cbranch_scc0 .Lslowout_0
.LBB0_139:
	s_lshr_b32 s8, s8, 16
	s_and_b32 s19, s6, 0xffff0000
	s_mov_b32 s25, 0
	s_lshl_b64 s[26:27], s[4:5], 16
	s_or_b32 s24, s19, s8
	s_and_b32 s27, s27, 0xffff
	s_mov_b32 s26, s25
	s_or_b64 s[26:27], s[24:25], s[26:27]
	s_and_b32 s31, s0, 0xffff0000
	s_mov_b32 s30, s25
	s_or_b64 s[26:27], s[26:27], s[30:31]
	s_add_u32 s30, s26, -1
	s_addc_u32 s31, s27, -1
	s_and_b64 s[30:31], s[26:27], s[30:31]
	s_cmp_eq_u64 s[30:31], 0
	v_readlane_b32 s8, v14, 16
	s_cbranch_scc0 .Lslowout_1
.LBB0_142:
	s_mov_b32 s25, 0
	s_lshr_b64 s[26:27], s[6:7], 16
	s_and_b32 s24, s9, 0xffff
	s_and_b32 s26, s26, 0xffff0000
	s_mov_b32 s27, s25
	s_or_b64 s[26:27], s[26:27], s[24:25]
	s_and_b32 s31, s5, 0xffff
	s_mov_b32 s30, s25
	s_or_b64 s[26:27], s[26:27], s[30:31]
	s_lshl_b64 s[30:31], s[0:1], 16
	s_and_b32 s31, s31, 0xffff0000
	s_mov_b32 s30, s25
	s_or_b64 s[26:27], s[26:27], s[30:31]
	s_add_u32 s30, s26, -1
	s_addc_u32 s31, s27, -1
	s_and_b64 s[30:31], s[26:27], s[30:31]
	s_cmp_eq_u64 s[30:31], 0
	v_readlane_b32 s0, v14, 32
	s_cbranch_scc0 .Lslowout_2
.LBB0_145:
	s_mov_b32 s25, 0
	s_lshr_b32 s24, s9, 16
	s_and_b32 s6, s7, 0xffff0000
	s_mov_b32 s7, s25
	s_lshr_b64 s[4:5], s[4:5], 16
	s_or_b64 s[6:7], s[6:7], s[24:25]
	s_mov_b32 s4, s25
	s_or_b64 s[4:5], s[6:7], s[4:5]
	s_and_b32 s7, s1, 0xffff0000
	s_mov_b32 s6, s25
	s_or_b64 s[6:7], s[4:5], s[6:7]
	s_add_u32 s4, s6, -1
	s_addc_u32 s5, s7, -1
	s_and_b64 s[4:5], s[6:7], s[4:5]
	s_cmp_eq_u64 s[4:5], 0
	v_readlane_b32 s4, v14, 48
	s_cbranch_scc0 .Lslowout_3

.LBB0_170:
	v_mov_b32_e32 v0, 0x111a0
	v_mov_b32_e32 v4, 0x111b0
	ds_read_b128 v[0:3], v0
	ds_read_b128 v[4:7], v4
	s_mov_b32 s17, 0
	s_lshl_b64 s[0:1], s[16:17], 3
	s_add_u32 s0, s14, s0
	s_waitcnt lgkmcnt(1)
	v_add_f64 v[0:1], v[0:1], v[2:3]
	s_waitcnt lgkmcnt(0)
	v_add_f64 v[2:3], v[4:5], v[6:7]
	v_add_f64 v[0:1], v[0:1], v[2:3]
	v_ldexp_f64 v[4:5], v[0:1], -8
	v_mov_b32_e32 v0, 0x11150
	ds_read_b128 v[0:3], v0
	s_addc_u32 s1, s15, s1
	v_mov_b32_e32 v6, 0
	global_store_dwordx2 v6, v[4:5], s[0:1]
	s_lshl_b32 s0, s16, 2
	s_waitcnt lgkmcnt(0)
	v_add_u32_e32 v0, v1, v0
	v_add_u32_e32 v0, v0, v2
	v_add_u32_e32 v0, v0, v3
	v_mov_b32_e32 v1, s0
	global_store_dword v1, v0, s[10:11]
	s_endpgm
.Lslowout_0:
	s_lshl_b32 s19, s29, 2
	s_add_i32 s19, s19, 0x11100
	v_mov_b32_e32 v4, s19
	ds_read_b32 v4, v4
	s_mul_i32 s19, s17, 0x2040
	v_add_u32_e32 v8, s19, v135
	v_mov_b32_e32 v15, 0x7f800000
	s_waitcnt lgkmcnt(0)
	v_max_i32_e32 v4, 1, v4
	v_cvt_f64_u32_e32 v[12:13], v4
	v_div_scale_f64 v[16:17], s[30:31], v[12:13], v[12:13], 1.0
	v_rcp_f64_e32 v[20:21], v[16:17]
	v_div_scale_f64 v[22:23], vcc, 1.0, v[12:13], 1.0
	ds_read2st64_b64 v[4:7], v8 offset0:64 offset1:65
	ds_read2st64_b64 v[8:11], v8 offset0:66 offset1:67
	v_fma_f64 v[24:25], -v[16:17], v[20:21], 1.0
	v_fmac_f64_e32 v[20:21], v[20:21], v[24:25]
	v_fma_f64 v[24:25], -v[16:17], v[20:21], 1.0
	v_fmac_f64_e32 v[20:21], v[20:21], v[24:25]
	v_mul_f64 v[24:25], v[22:23], v[20:21]
	v_fma_f64 v[16:17], -v[16:17], v[24:25], v[22:23]
	v_div_fmas_f64 v[16:17], v[16:17], v[20:21], v[24:25]
	v_div_fixup_f64 v[12:13], v[16:17], v[12:13], 1.0
	s_waitcnt lgkmcnt(1)
	v_mul_f64 v[6:7], v[6:7], v[12:13]
	v_mul_f64 v[4:5], v[4:5], v[12:13]
	s_waitcnt lgkmcnt(0)
	v_mul_f64 v[8:9], v[8:9], v[12:13]
	v_mul_f64 v[10:11], v[12:13], v[10:11]
	v_mul_f64 v[12:13], v[6:7], v[6:7]
	v_fmac_f64_e32 v[12:13], v[4:5], v[4:5]
	v_fmac_f64_e32 v[12:13], v[8:9], v[8:9]
	v_fmac_f64_e32 v[12:13], v[10:11], v[10:11]
	s_nop 1
	v_mov_b32_dpp v16, v12 quad_perm:[1,0,3,2] row_mask:0xf bank_mask:0xf bound_ctrl:1
	v_mov_b32_dpp v17, v13 quad_perm:[1,0,3,2] row_mask:0xf bank_mask:0xf bound_ctrl:1
	v_add_f64 v[12:13], v[12:13], v[16:17]
	s_nop 1
	v_mov_b32_dpp v16, v12 quad_perm:[2,3,0,1] row_mask:0xf bank_mask:0xf bound_ctrl:1
	v_mov_b32_dpp v17, v13 quad_perm:[2,3,0,1] row_mask:0xf bank_mask:0xf bound_ctrl:1
	v_add_f64 v[12:13], v[12:13], v[16:17]
	s_nop 1
	v_mov_b32_dpp v16, v12 row_half_mirror row_mask:0xf bank_mask:0xf bound_ctrl:1
	v_mov_b32_dpp v17, v13 row_half_mirror row_mask:0xf bank_mask:0xf bound_ctrl:1
	v_add_f64 v[12:13], v[12:13], v[16:17]
	s_nop 1
	v_mov_b32_dpp v16, v12 row_mirror row_mask:0xf bank_mask:0xf bound_ctrl:1
	v_mov_b32_dpp v17, v13 row_mirror row_mask:0xf bank_mask:0xf bound_ctrl:1
	v_add_f64 v[12:13], v[12:13], v[16:17]
	s_nop 0
	v_readlane_b32 s19, v13, 16
	v_readlane_b32 s23, v12, 16
	v_readlane_b32 s31, v13, 0
	v_readlane_b32 s30, v12, 0
	v_mov_b32_e32 v16, s23
	v_mov_b32_e32 v17, s19
	v_readlane_b32 s19, v13, 48
	v_readlane_b32 s23, v12, 48
	v_add_f64 v[16:17], s[30:31], v[16:17]
	v_readlane_b32 s31, v13, 32
	v_readlane_b32 s30, v12, 32
	v_mov_b32_e32 v12, s23
	v_mov_b32_e32 v13, s19
	v_add_f64 v[12:13], s[30:31], v[12:13]
	v_add_f64 v[12:13], v[16:17], v[12:13]
.LBB0_138:
	s_ff1_i32_b64 s19, s[26:27]
	s_add_u32 s30, s26, -1
	s_addc_u32 s31, s27, -1
	s_lshl_b32 s24, s19, 10
	v_lshl_add_u64 v[16:17], v[2:3], 0, s[24:25]
	global_load_dwordx4 v[20:23], v[16:17], off
	s_and_b64 s[26:27], s[30:31], s[26:27]
	s_waitcnt vmcnt(0)
	v_cvt_f64_f32_e32 v[16:17], v20
	v_cvt_f64_f32_e32 v[20:21], v21
	v_mul_f64 v[26:27], v[6:7], v[20:21]
	v_mul_f64 v[20:21], v[20:21], v[20:21]
	v_cvt_f64_f32_e32 v[24:25], v22
	v_fmac_f64_e32 v[26:27], v[4:5], v[16:17]
	v_fmac_f64_e32 v[20:21], v[16:17], v[16:17]
	v_cvt_f64_f32_e32 v[22:23], v23
	v_fmac_f64_e32 v[26:27], v[8:9], v[24:25]
	v_fmac_f64_e32 v[20:21], v[24:25], v[24:25]
	v_fmac_f64_e32 v[26:27], v[10:11], v[22:23]
	v_fmac_f64_e32 v[20:21], v[22:23], v[22:23]
	s_nop 0
	v_mov_b32_dpp v16, v26 quad_perm:[1,0,3,2] row_mask:0xf bank_mask:0xf bound_ctrl:1
	v_mov_b32_dpp v17, v27 quad_perm:[1,0,3,2] row_mask:0xf bank_mask:0xf bound_ctrl:1
	v_mov_b32_dpp v22, v20 quad_perm:[1,0,3,2] row_mask:0xf bank_mask:0xf bound_ctrl:1
	v_mov_b32_dpp v23, v21 quad_perm:[1,0,3,2] row_mask:0xf bank_mask:0xf bound_ctrl:1
	v_add_f64 v[16:17], v[26:27], v[16:17]
	v_add_f64 v[20:21], v[20:21], v[22:23]
	s_nop 0
	v_mov_b32_dpp v22, v16 quad_perm:[2,3,0,1] row_mask:0xf bank_mask:0xf bound_ctrl:1
	v_mov_b32_dpp v23, v17 quad_perm:[2,3,0,1] row_mask:0xf bank_mask:0xf bound_ctrl:1
	v_mov_b32_dpp v24, v20 quad_perm:[2,3,0,1] row_mask:0xf bank_mask:0xf bound_ctrl:1
	v_mov_b32_dpp v25, v21 quad_perm:[2,3,0,1] row_mask:0xf bank_mask:0xf bound_ctrl:1
	v_add_f64 v[16:17], v[16:17], v[22:23]
	v_add_f64 v[20:21], v[20:21], v[24:25]
	s_nop 0
	v_mov_b32_dpp v22, v16 row_half_mirror row_mask:0xf bank_mask:0xf bound_ctrl:1
	v_mov_b32_dpp v23, v17 row_half_mirror row_mask:0xf bank_mask:0xf bound_ctrl:1
	v_mov_b32_dpp v24, v20 row_half_mirror row_mask:0xf bank_mask:0xf bound_ctrl:1
	v_mov_b32_dpp v25, v21 row_half_mirror row_mask:0xf bank_mask:0xf bound_ctrl:1
	v_add_f64 v[16:17], v[16:17], v[22:23]
	v_add_f64 v[20:21], v[20:21], v[24:25]
	s_nop 0
	v_mov_b32_dpp v22, v16 row_mirror row_mask:0xf bank_mask:0xf bound_ctrl:1
	v_mov_b32_dpp v23, v17 row_mirror row_mask:0xf bank_mask:0xf bound_ctrl:1
	v_mov_b32_dpp v24, v20 row_mirror row_mask:0xf bank_mask:0xf bound_ctrl:1
	v_mov_b32_dpp v25, v21 row_mirror row_mask:0xf bank_mask:0xf bound_ctrl:1
	v_add_f64 v[16:17], v[16:17], v[22:23]
	v_add_f64 v[20:21], v[20:21], v[24:25]
	v_readlane_b32 s23, v17, 16
	v_readlane_b32 s24, v16, 16
	v_readlane_b32 s33, v17, 48
	v_readlane_b32 s40, v16, 48
	v_readlane_b32 s41, v21, 16
	v_readlane_b32 s42, v20, 16
	v_readlane_b32 s43, v21, 48
	v_readlane_b32 s44, v20, 48
	v_readlane_b32 s31, v17, 0
	v_readlane_b32 s30, v16, 0
	v_readlane_b32 s35, v17, 32
	v_readlane_b32 s34, v16, 32
	v_readlane_b32 s37, v21, 0
	v_readlane_b32 s36, v20, 0
	v_readlane_b32 s39, v21, 32
	v_readlane_b32 s38, v20, 32
	v_mov_b32_e32 v16, s24
	v_mov_b32_e32 v17, s23
	v_mov_b32_e32 v20, s40
	v_mov_b32_e32 v21, s33
	v_mov_b32_e32 v22, s42
	v_mov_b32_e32 v23, s41
	v_mov_b32_e32 v24, s44
	v_mov_b32_e32 v25, s43
	v_add_f64 v[16:17], s[30:31], v[16:17]
	v_add_f64 v[20:21], s[34:35], v[20:21]
	v_add_f64 v[22:23], s[36:37], v[22:23]
	v_add_f64 v[24:25], s[38:39], v[24:25]
	v_add_f64 v[16:17], v[16:17], v[20:21]
	v_add_f64 v[20:21], v[22:23], v[24:25]
	v_add_f64 v[20:21], v[12:13], v[20:21]
	v_fmac_f64_e32 v[20:21], -2.0, v[16:17]
	v_cvt_f32_f64_e32 v16, v[20:21]
	v_cmp_gt_f32_e32 vcc, v15, v16
	s_and_b64 s[30:31], vcc, exec
	s_cselect_b32 s22, s19, s22
	v_cndmask_b32_e32 v15, v15, v16, vcc
	s_cmp_lg_u64 s[26:27], 0
	s_cbranch_scc1 .LBB0_138
	s_branch .LBB0_139

.LBB0_141:
	s_ff1_i32_b64 s19, s[26:27]
	s_add_u32 s30, s26, -1
	s_addc_u32 s31, s27, -1
	s_lshl_b32 s24, s19, 10
	v_lshl_add_u64 v[16:17], v[2:3], 0, s[24:25]
	global_load_dwordx4 v[20:23], v[16:17], off
	s_and_b64 s[26:27], s[30:31], s[26:27]
	s_waitcnt vmcnt(0)
	v_cvt_f64_f32_e32 v[16:17], v20
	v_cvt_f64_f32_e32 v[20:21], v21
	v_mul_f64 v[26:27], v[6:7], v[20:21]
	v_mul_f64 v[20:21], v[20:21], v[20:21]
	v_cvt_f64_f32_e32 v[24:25], v22
	v_fmac_f64_e32 v[26:27], v[4:5], v[16:17]
	v_fmac_f64_e32 v[20:21], v[16:17], v[16:17]
	v_cvt_f64_f32_e32 v[22:23], v23
	v_fmac_f64_e32 v[26:27], v[8:9], v[24:25]
	v_fmac_f64_e32 v[20:21], v[24:25], v[24:25]
	v_fmac_f64_e32 v[26:27], v[10:11], v[22:23]
	v_fmac_f64_e32 v[20:21], v[22:23], v[22:23]
	s_nop 0
	v_mov_b32_dpp v16, v26 quad_perm:[1,0,3,2] row_mask:0xf bank_mask:0xf bound_ctrl:1
	v_mov_b32_dpp v17, v27 quad_perm:[1,0,3,2] row_mask:0xf bank_mask:0xf bound_ctrl:1
	v_mov_b32_dpp v22, v20 quad_perm:[1,0,3,2] row_mask:0xf bank_mask:0xf bound_ctrl:1
	v_mov_b32_dpp v23, v21 quad_perm:[1,0,3,2] row_mask:0xf bank_mask:0xf bound_ctrl:1
	v_add_f64 v[16:17], v[26:27], v[16:17]
	v_add_f64 v[20:21], v[20:21], v[22:23]
	s_nop 0
	v_mov_b32_dpp v22, v16 quad_perm:[2,3,0,1] row_mask:0xf bank_mask:0xf bound_ctrl:1
	v_mov_b32_dpp v23, v17 quad_perm:[2,3,0,1] row_mask:0xf bank_mask:0xf bound_ctrl:1
	v_mov_b32_dpp v24, v20 quad_perm:[2,3,0,1] row_mask:0xf bank_mask:0xf bound_ctrl:1
	v_mov_b32_dpp v25, v21 quad_perm:[2,3,0,1] row_mask:0xf bank_mask:0xf bound_ctrl:1
	v_add_f64 v[16:17], v[16:17], v[22:23]
	v_add_f64 v[20:21], v[20:21], v[24:25]
	s_nop 0
	v_mov_b32_dpp v22, v16 row_half_mirror row_mask:0xf bank_mask:0xf bound_ctrl:1
	v_mov_b32_dpp v23, v17 row_half_mirror row_mask:0xf bank_mask:0xf bound_ctrl:1
	v_mov_b32_dpp v24, v20 row_half_mirror row_mask:0xf bank_mask:0xf bound_ctrl:1
	v_mov_b32_dpp v25, v21 row_half_mirror row_mask:0xf bank_mask:0xf bound_ctrl:1
	v_add_f64 v[16:17], v[16:17], v[22:23]
	v_add_f64 v[20:21], v[20:21], v[24:25]
	s_nop 0
	v_mov_b32_dpp v22, v16 row_mirror row_mask:0xf bank_mask:0xf bound_ctrl:1
	v_mov_b32_dpp v23, v17 row_mirror row_mask:0xf bank_mask:0xf bound_ctrl:1
	v_mov_b32_dpp v24, v20 row_mirror row_mask:0xf bank_mask:0xf bound_ctrl:1
	v_mov_b32_dpp v25, v21 row_mirror row_mask:0xf bank_mask:0xf bound_ctrl:1
	v_add_f64 v[16:17], v[16:17], v[22:23]
	v_add_f64 v[20:21], v[20:21], v[24:25]
	v_readlane_b32 s23, v17, 16
	v_readlane_b32 s24, v16, 16
	v_readlane_b32 s33, v17, 48
	v_readlane_b32 s40, v16, 48
	v_readlane_b32 s41, v21, 16
	v_readlane_b32 s42, v20, 16
	v_readlane_b32 s43, v21, 48
	v_readlane_b32 s44, v20, 48
	v_readlane_b32 s31, v17, 0
	v_readlane_b32 s30, v16, 0
	v_readlane_b32 s35, v17, 32
	v_readlane_b32 s34, v16, 32
	v_readlane_b32 s37, v21, 0
	v_readlane_b32 s36, v20, 0
	v_readlane_b32 s39, v21, 32
	v_readlane_b32 s38, v20, 32
	v_mov_b32_e32 v16, s24
	v_mov_b32_e32 v17, s23
	v_mov_b32_e32 v20, s40
	v_mov_b32_e32 v21, s33
	v_mov_b32_e32 v22, s42
	v_mov_b32_e32 v23, s41
	v_mov_b32_e32 v24, s44
	v_mov_b32_e32 v25, s43
	v_add_f64 v[16:17], s[30:31], v[16:17]
	v_add_f64 v[20:21], s[34:35], v[20:21]
	v_add_f64 v[22:23], s[36:37], v[22:23]
	v_add_f64 v[24:25], s[38:39], v[24:25]
	v_add_f64 v[16:17], v[16:17], v[20:21]
	v_add_f64 v[20:21], v[22:23], v[24:25]
	v_add_f64 v[20:21], v[12:13], v[20:21]
	v_fmac_f64_e32 v[20:21], -2.0, v[16:17]
	v_cvt_f32_f64_e32 v16, v[20:21]
	v_cmp_gt_f32_e32 vcc, v15, v16
	s_and_b64 s[30:31], vcc, exec
	s_cselect_b32 s8, s19, s8
	v_cndmask_b32_e32 v15, v15, v16, vcc
	s_cmp_lg_u64 s[26:27], 0
	s_cbranch_scc1 .LBB0_141
	s_branch .LBB0_142

.LBB0_144:
	s_ff1_i32_b64 s6, s[26:27]
	s_add_u32 s30, s26, -1
	s_addc_u32 s31, s27, -1
	s_lshl_b32 s24, s6, 10
	v_lshl_add_u64 v[16:17], v[2:3], 0, s[24:25]
	global_load_dwordx4 v[20:23], v[16:17], off
	s_and_b64 s[26:27], s[30:31], s[26:27]
	s_waitcnt vmcnt(0)
	v_cvt_f64_f32_e32 v[16:17], v20
	v_cvt_f64_f32_e32 v[20:21], v21
	v_mul_f64 v[26:27], v[6:7], v[20:21]
	v_mul_f64 v[20:21], v[20:21], v[20:21]
	v_cvt_f64_f32_e32 v[24:25], v22
	v_fmac_f64_e32 v[26:27], v[4:5], v[16:17]
	v_fmac_f64_e32 v[20:21], v[16:17], v[16:17]
	v_cvt_f64_f32_e32 v[22:23], v23
	v_fmac_f64_e32 v[26:27], v[8:9], v[24:25]
	v_fmac_f64_e32 v[20:21], v[24:25], v[24:25]
	v_fmac_f64_e32 v[26:27], v[10:11], v[22:23]
	v_fmac_f64_e32 v[20:21], v[22:23], v[22:23]
	s_nop 0
	v_mov_b32_dpp v16, v26 quad_perm:[1,0,3,2] row_mask:0xf bank_mask:0xf bound_ctrl:1
	v_mov_b32_dpp v17, v27 quad_perm:[1,0,3,2] row_mask:0xf bank_mask:0xf bound_ctrl:1
	v_mov_b32_dpp v22, v20 quad_perm:[1,0,3,2] row_mask:0xf bank_mask:0xf bound_ctrl:1
	v_mov_b32_dpp v23, v21 quad_perm:[1,0,3,2] row_mask:0xf bank_mask:0xf bound_ctrl:1
	v_add_f64 v[16:17], v[26:27], v[16:17]
	v_add_f64 v[20:21], v[20:21], v[22:23]
	s_nop 0
	v_mov_b32_dpp v22, v16 quad_perm:[2,3,0,1] row_mask:0xf bank_mask:0xf bound_ctrl:1
	v_mov_b32_dpp v23, v17 quad_perm:[2,3,0,1] row_mask:0xf bank_mask:0xf bound_ctrl:1
	v_mov_b32_dpp v24, v20 quad_perm:[2,3,0,1] row_mask:0xf bank_mask:0xf bound_ctrl:1
	v_mov_b32_dpp v25, v21 quad_perm:[2,3,0,1] row_mask:0xf bank_mask:0xf bound_ctrl:1
	v_add_f64 v[16:17], v[16:17], v[22:23]
	v_add_f64 v[20:21], v[20:21], v[24:25]
	s_nop 0
	v_mov_b32_dpp v22, v16 row_half_mirror row_mask:0xf bank_mask:0xf bound_ctrl:1
	v_mov_b32_dpp v23, v17 row_half_mirror row_mask:0xf bank_mask:0xf bound_ctrl:1
	v_mov_b32_dpp v24, v20 row_half_mirror row_mask:0xf bank_mask:0xf bound_ctrl:1
	v_mov_b32_dpp v25, v21 row_half_mirror row_mask:0xf bank_mask:0xf bound_ctrl:1
	v_add_f64 v[16:17], v[16:17], v[22:23]
	v_add_f64 v[20:21], v[20:21], v[24:25]
	s_nop 0
	v_mov_b32_dpp v22, v16 row_mirror row_mask:0xf bank_mask:0xf bound_ctrl:1
	v_mov_b32_dpp v23, v17 row_mirror row_mask:0xf bank_mask:0xf bound_ctrl:1
	v_mov_b32_dpp v24, v20 row_mirror row_mask:0xf bank_mask:0xf bound_ctrl:1
	v_mov_b32_dpp v25, v21 row_mirror row_mask:0xf bank_mask:0xf bound_ctrl:1
	v_add_f64 v[16:17], v[16:17], v[22:23]
	v_add_f64 v[20:21], v[20:21], v[24:25]
	v_readlane_b32 s19, v17, 16
	v_readlane_b32 s23, v16, 16
	v_readlane_b32 s24, v17, 48
	v_readlane_b32 s33, v16, 48
	v_readlane_b32 s40, v21, 16
	v_readlane_b32 s41, v20, 16
	v_readlane_b32 s42, v21, 48
	v_readlane_b32 s43, v20, 48
	v_readlane_b32 s31, v17, 0
	v_readlane_b32 s30, v16, 0
	v_readlane_b32 s35, v17, 32
	v_readlane_b32 s34, v16, 32
	v_readlane_b32 s37, v21, 0
	v_readlane_b32 s36, v20, 0
	v_readlane_b32 s39, v21, 32
	v_readlane_b32 s38, v20, 32
	v_mov_b32_e32 v16, s23
	v_mov_b32_e32 v17, s19
	v_mov_b32_e32 v20, s33
	v_mov_b32_e32 v21, s24
	v_mov_b32_e32 v22, s41
	v_mov_b32_e32 v23, s40
	v_mov_b32_e32 v24, s43
	v_mov_b32_e32 v25, s42
	v_add_f64 v[16:17], s[30:31], v[16:17]
	v_add_f64 v[20:21], s[34:35], v[20:21]
	v_add_f64 v[22:23], s[36:37], v[22:23]
	v_add_f64 v[24:25], s[38:39], v[24:25]
	v_add_f64 v[16:17], v[16:17], v[20:21]
	v_add_f64 v[20:21], v[22:23], v[24:25]
	v_add_f64 v[20:21], v[12:13], v[20:21]
	v_fmac_f64_e32 v[20:21], -2.0, v[16:17]
	v_cvt_f32_f64_e32 v16, v[20:21]
	v_cmp_gt_f32_e32 vcc, v15, v16
	s_and_b64 s[30:31], vcc, exec
	s_cselect_b32 s0, s6, s0
	v_cndmask_b32_e32 v15, v15, v16, vcc
	s_cmp_lg_u64 s[26:27], 0
	s_cbranch_scc1 .LBB0_144
	s_branch .LBB0_145

.LBB0_147:
	s_ff1_i32_b64 s1, s[6:7]
	s_add_u32 s26, s6, -1
	s_addc_u32 s27, s7, -1
	s_lshl_b32 s24, s1, 10
	v_lshl_add_u64 v[16:17], v[2:3], 0, s[24:25]
	global_load_dwordx4 v[20:23], v[16:17], off
	s_and_b64 s[6:7], s[26:27], s[6:7]
	s_waitcnt vmcnt(0)
	v_cvt_f64_f32_e32 v[16:17], v20
	v_cvt_f64_f32_e32 v[20:21], v21
	v_mul_f64 v[26:27], v[6:7], v[20:21]
	v_mul_f64 v[20:21], v[20:21], v[20:21]
	v_cvt_f64_f32_e32 v[24:25], v22
	v_fmac_f64_e32 v[26:27], v[4:5], v[16:17]
	v_fmac_f64_e32 v[20:21], v[16:17], v[16:17]
	v_cvt_f64_f32_e32 v[22:23], v23
	v_fmac_f64_e32 v[26:27], v[8:9], v[24:25]
	v_fmac_f64_e32 v[20:21], v[24:25], v[24:25]
	v_fmac_f64_e32 v[26:27], v[10:11], v[22:23]
	v_fmac_f64_e32 v[20:21], v[22:23], v[22:23]
	s_nop 0
	v_mov_b32_dpp v16, v26 quad_perm:[1,0,3,2] row_mask:0xf bank_mask:0xf bound_ctrl:1
	v_mov_b32_dpp v17, v27 quad_perm:[1,0,3,2] row_mask:0xf bank_mask:0xf bound_ctrl:1
	v_mov_b32_dpp v22, v20 quad_perm:[1,0,3,2] row_mask:0xf bank_mask:0xf bound_ctrl:1
	v_mov_b32_dpp v23, v21 quad_perm:[1,0,3,2] row_mask:0xf bank_mask:0xf bound_ctrl:1
	v_add_f64 v[16:17], v[26:27], v[16:17]
	v_add_f64 v[20:21], v[20:21], v[22:23]
	s_nop 0
	v_mov_b32_dpp v22, v16 quad_perm:[2,3,0,1] row_mask:0xf bank_mask:0xf bound_ctrl:1
	v_mov_b32_dpp v23, v17 quad_perm:[2,3,0,1] row_mask:0xf bank_mask:0xf bound_ctrl:1
	v_mov_b32_dpp v24, v20 quad_perm:[2,3,0,1] row_mask:0xf bank_mask:0xf bound_ctrl:1
	v_mov_b32_dpp v25, v21 quad_perm:[2,3,0,1] row_mask:0xf bank_mask:0xf bound_ctrl:1
	v_add_f64 v[16:17], v[16:17], v[22:23]
	v_add_f64 v[20:21], v[20:21], v[24:25]
	s_nop 0
	v_mov_b32_dpp v22, v16 row_half_mirror row_mask:0xf bank_mask:0xf bound_ctrl:1
	v_mov_b32_dpp v23, v17 row_half_mirror row_mask:0xf bank_mask:0xf bound_ctrl:1
	v_mov_b32_dpp v24, v20 row_half_mirror row_mask:0xf bank_mask:0xf bound_ctrl:1
	v_mov_b32_dpp v25, v21 row_half_mirror row_mask:0xf bank_mask:0xf bound_ctrl:1
	v_add_f64 v[16:17], v[16:17], v[22:23]
	v_add_f64 v[20:21], v[20:21], v[24:25]
	s_nop 0
	v_mov_b32_dpp v22, v16 row_mirror row_mask:0xf bank_mask:0xf bound_ctrl:1
	v_mov_b32_dpp v23, v17 row_mirror row_mask:0xf bank_mask:0xf bound_ctrl:1
	v_mov_b32_dpp v24, v20 row_mirror row_mask:0xf bank_mask:0xf bound_ctrl:1
	v_mov_b32_dpp v25, v21 row_mirror row_mask:0xf bank_mask:0xf bound_ctrl:1
	v_add_f64 v[16:17], v[16:17], v[22:23]
	v_add_f64 v[20:21], v[20:21], v[24:25]
	v_readlane_b32 s5, v17, 16
	v_readlane_b32 s9, v16, 16
	v_readlane_b32 s19, v17, 48
	v_readlane_b32 s23, v16, 48
	v_readlane_b32 s24, v21, 16
	v_readlane_b32 s33, v20, 16
	v_readlane_b32 s38, v21, 48
	v_readlane_b32 s39, v20, 48
	v_readlane_b32 s27, v17, 0
	v_readlane_b32 s26, v16, 0
	v_readlane_b32 s31, v17, 32
	v_readlane_b32 s30, v16, 32
	v_readlane_b32 s35, v21, 0
	v_readlane_b32 s34, v20, 0
	v_readlane_b32 s37, v21, 32
	v_readlane_b32 s36, v20, 32
	v_mov_b32_e32 v16, s9
	v_mov_b32_e32 v17, s5
	v_mov_b32_e32 v20, s23
	v_mov_b32_e32 v21, s19
	v_mov_b32_e32 v22, s33
	v_mov_b32_e32 v23, s24
	v_mov_b32_e32 v24, s39
	v_mov_b32_e32 v25, s38
	v_add_f64 v[16:17], s[26:27], v[16:17]
	v_add_f64 v[20:21], s[30:31], v[20:21]
	v_add_f64 v[22:23], s[34:35], v[22:23]
	v_add_f64 v[24:25], s[36:37], v[24:25]
	v_add_f64 v[16:17], v[16:17], v[20:21]
	v_add_f64 v[20:21], v[22:23], v[24:25]
	v_add_f64 v[20:21], v[12:13], v[20:21]
	v_fmac_f64_e32 v[20:21], -2.0, v[16:17]
	v_cvt_f32_f64_e32 v15, v[20:21]
	v_cmp_gt_f32_e32 vcc, v14, v15
	s_and_b64 s[26:27], vcc, exec
	s_cselect_b32 s4, s1, s4
	v_cndmask_b32_e32 v14, v14, v15, vcc
	s_cmp_lg_u64 s[6:7], 0
	s_cbranch_scc1 .LBB0_147
	s_branch .LBB0_148
